# grid barrier: last arriver of each XCD adds to the top counter without return and polls it like the rest (no generation word, no division)
# speedup vs baseline: 1.0012x; 1.0012x over previous
.LBB0_253:
	s_andn2_saveexec_b64 s[2:3], s[2:3]
	s_cbranch_execz .LBB0_271
	buffer_wbl2 sc1
	v_readlane_b32 s6, v255, 9
	v_readlane_b32 s7, v255, 10
	v_mov_b32_e32 v6, 0x20164
	ds_read_b32 v6, v6
	s_waitcnt vmcnt(0) lgkmcnt(0)
	v_add_u32_e32 v3, 1, v3
	v_mul_lo_u32 v3, v3, v6
	v_mov_b32_e32 v6, 0x3000
	v_mov_b32_e32 v5, 1
	s_mov_b32 s10, 0
	global_atomic_add v6, v5, s[6:7] offset:1024
.Lxbl_spin_0:
	global_load_dword v5, v6, s[6:7] offset:1024 sc1
	s_waitcnt vmcnt(0)
	v_cmp_ge_u32_e32 vcc, v5, v3
	s_cbranch_vccnz .Lxbl_done_0
	s_sleep 1
	s_add_u32 s10, s10, 1
	s_cmp_lt_u32 s10, 0x40000
	s_cbranch_scc1 .Lxbl_spin_0
.Lxbl_done_0:
.LBB0_271:
	s_or_b64 exec, exec, s[4:5]
	s_waitcnt lgkmcnt(0)
	s_barrier

.LBB0_852:
	s_andn2_saveexec_b64 s[6:7], s[6:7]
	s_cbranch_execz .LBB0_870
	buffer_wbl2 sc1
	v_readlane_b32 s16, v255, 9
	v_readlane_b32 s17, v255, 10
	v_mov_b32_e32 v6, 0x20164
	ds_read_b32 v6, v6
	s_waitcnt vmcnt(0) lgkmcnt(0)
	v_add_u32_e32 v3, 1, v3
	v_mul_lo_u32 v3, v3, v6
	v_mov_b32_e32 v6, 0x3000
	v_mov_b32_e32 v5, 1
	s_mov_b32 s8, 0
	global_atomic_add v6, v5, s[16:17] offset:1024
.Lxbl_spin_2:
	global_load_dword v5, v6, s[16:17] offset:1024 sc1
	s_waitcnt vmcnt(0)
	v_cmp_ge_u32_e32 vcc, v5, v3
	s_cbranch_vccnz .Lxbl_done_2
	s_sleep 1
	s_add_u32 s8, s8, 1
	s_cmp_lt_u32 s8, 0x40000
	s_cbranch_scc1 .Lxbl_spin_2

.LBB0_932:
	s_andn2_saveexec_b64 s[6:7], s[6:7]
	s_cbranch_execz .LBB0_950
	buffer_wbl2 sc1
	v_readlane_b32 s8, v255, 9
	v_readlane_b32 s9, v255, 10
	v_mov_b32_e32 v6, 0x20164
	ds_read_b32 v6, v6
	s_waitcnt vmcnt(0) lgkmcnt(0)
	v_add_u32_e32 v3, 1, v3
	v_mul_lo_u32 v3, v3, v6
	v_mov_b32_e32 v6, 0x3000
	v_mov_b32_e32 v5, 1
	s_mov_b32 s10, 0
	global_atomic_add v6, v5, s[8:9] offset:1024
.Lxbl_spin_3:
	global_load_dword v5, v6, s[8:9] offset:1024 sc1
	s_waitcnt vmcnt(0)
	v_cmp_ge_u32_e32 vcc, v5, v3
	s_cbranch_vccnz .Lxbl_done_3
	s_sleep 1
	s_add_u32 s10, s10, 1
	s_cmp_lt_u32 s10, 0x40000
	s_cbranch_scc1 .Lxbl_spin_3

.LBB0_1012:
	s_andn2_saveexec_b64 s[6:7], s[6:7]
	s_cbranch_execz .LBB0_1030
	buffer_wbl2 sc1
	v_readlane_b32 s8, v255, 9
	v_readlane_b32 s9, v255, 10
	v_mov_b32_e32 v70, 0x20164
	ds_read_b32 v70, v70
	s_waitcnt vmcnt(0) lgkmcnt(0)
	v_add_u32_e32 v67, 1, v67
	v_mul_lo_u32 v67, v67, v70
	v_mov_b32_e32 v70, 0x3000
	v_mov_b32_e32 v69, 1
	s_mov_b32 s24, 0
	global_atomic_add v70, v69, s[8:9] offset:1024
.Lxbl_spin_4:
	global_load_dword v69, v70, s[8:9] offset:1024 sc1
	s_waitcnt vmcnt(0)
	v_cmp_ge_u32_e32 vcc, v69, v67
	s_cbranch_vccnz .Lxbl_done_4
	s_sleep 1
	s_add_u32 s24, s24, 1
	s_cmp_lt_u32 s24, 0x40000
	s_cbranch_scc1 .Lxbl_spin_4
.Lxbl_done_4:
.LBB0_1030:
	s_or_b64 exec, exec, s[0:1]
	s_waitcnt lgkmcnt(0)
	s_barrier

.LBB0_1152:
	s_andn2_saveexec_b64 s[4:5], s[4:5]
	s_cbranch_execz .LBB0_1170
	buffer_wbl2 sc1
	v_readlane_b32 s6, v255, 9
	v_readlane_b32 s7, v255, 10
	v_mov_b32_e32 v6, 0x20164
	ds_read_b32 v6, v6
	s_waitcnt vmcnt(0) lgkmcnt(0)
	v_add_u32_e32 v3, 1, v3
	v_mul_lo_u32 v3, v3, v6
	v_mov_b32_e32 v6, 0x3000
	v_mov_b32_e32 v5, 1
	s_mov_b32 s22, 0
	global_atomic_add v6, v5, s[6:7] offset:1024
.Lxbl_spin_5:
	global_load_dword v5, v6, s[6:7] offset:1024 sc1
	s_waitcnt vmcnt(0)
	v_cmp_ge_u32_e32 vcc, v5, v3
	s_cbranch_vccnz .Lxbl_done_5
	s_sleep 1
	s_add_u32 s22, s22, 1
	s_cmp_lt_u32 s22, 0x40000
	s_cbranch_scc1 .Lxbl_spin_5

.LBB0_1265:
	s_andn2_saveexec_b64 s[2:3], s[2:3]
	s_cbranch_execz .LBB0_1283
	buffer_wbl2 sc1
	v_readlane_b32 s6, v255, 9
	v_readlane_b32 s7, v255, 10
	v_mov_b32_e32 v6, 0x20164
	ds_read_b32 v6, v6
	s_waitcnt vmcnt(0) lgkmcnt(0)
	v_add_u32_e32 v3, 1, v3
	v_mul_lo_u32 v3, v3, v6
	v_mov_b32_e32 v6, 0x3000
	v_mov_b32_e32 v5, 1
	s_mov_b32 s8, 0
	global_atomic_add v6, v5, s[6:7] offset:1024
.Lxbl_spin_6:
	global_load_dword v5, v6, s[6:7] offset:1024 sc1
	s_waitcnt vmcnt(0)
	v_cmp_ge_u32_e32 vcc, v5, v3
	s_cbranch_vccnz .Lxbl_done_6
	s_sleep 1
	s_add_u32 s8, s8, 1
	s_cmp_lt_u32 s8, 0x40000
	s_cbranch_scc1 .Lxbl_spin_6

.LBB0_1374:
	s_andn2_saveexec_b64 s[4:5], s[4:5]
	s_cbranch_execz .LBB0_1392
	buffer_wbl2 sc1
	v_readlane_b32 s6, v255, 9
	v_readlane_b32 s7, v255, 10
	v_mov_b32_e32 v4, 0x20164
	ds_read_b32 v4, v4
	s_waitcnt vmcnt(0) lgkmcnt(0)
	v_add_u32_e32 v1, 1, v1
	v_mul_lo_u32 v1, v1, v4
	v_mov_b32_e32 v4, 0x3000
	v_mov_b32_e32 v3, 1
	s_mov_b32 s24, 0
	global_atomic_add v4, v3, s[6:7] offset:1024
.Lxbl_spin_7:
	global_load_dword v3, v4, s[6:7] offset:1024 sc1
	s_waitcnt vmcnt(0)
	v_cmp_ge_u32_e32 vcc, v3, v1
	s_cbranch_vccnz .Lxbl_done_7
	s_sleep 1
	s_add_u32 s24, s24, 1
	s_cmp_lt_u32 s24, 0x40000
	s_cbranch_scc1 .Lxbl_spin_7
.Lxbl_done_7:
.LBB0_1392:
	s_or_b64 exec, exec, s[2:3]
	s_waitcnt lgkmcnt(0)
	s_barrier
